# out-projection loop header: the compiler's vmcnt(0) that drained the K-tile-1 stage loads (covered by the template's own counted waits) removed
# speedup vs baseline: 1.0056x; 1.0052x over previous
.LBB0_565:
	s_ashr_i32 s21, s20, 31
	s_lshl_b64 s[28:29], s[20:21], 19
	s_add_u32 s28, s33, s28
	s_addc_u32 s29, s42, s29
	s_and_b64 s[30:31], s[26:27], exec
	s_cselect_b32 s21, s29, s37
	s_cselect_b32 s56, s28, s36
	s_ashr_i32 s23, s22, 31
	s_lshl_b64 s[30:31], s[22:23], 19
	s_add_u32 s30, s43, s30
	s_addc_u32 s31, s44, s31
	s_and_b64 s[40:41], s[26:27], exec
	s_cselect_b32 s23, s31, s39
	s_cselect_b32 s57, s30, s38
	s_add_u32 s36, s36, 0x80
	s_addc_u32 s37, s37, 0
	s_add_u32 s58, s38, 0x100
	v_mov_b32_e32 v0, 0
	s_addc_u32 s59, s39, 0
	s_mov_b32 s60, -2
	s_nop 1
	v_mfma_f32_4x4x1_16b_f32 v[4:7], v0, v0, 0
	v_mfma_f32_4x4x1_16b_f32 v[8:11], v0, v0, 0
	v_mfma_f32_4x4x1_16b_f32 v[12:15], v0, v0, 0
	v_mfma_f32_4x4x1_16b_f32 v[16:19], v0, v0, 0
	v_mfma_f32_4x4x1_16b_f32 v[20:23], v0, v0, 0
	v_mfma_f32_4x4x1_16b_f32 v[24:27], v0, v0, 0
	v_mfma_f32_4x4x1_16b_f32 v[28:31], v0, v0, 0
	v_mfma_f32_4x4x1_16b_f32 v[32:35], v0, v0, 0
	v_mfma_f32_4x4x1_16b_f32 v[36:39], v0, v0, 0
	v_mfma_f32_4x4x1_16b_f32 v[40:43], v0, v0, 0
	v_mfma_f32_4x4x1_16b_f32 v[44:47], v0, v0, 0
	v_mfma_f32_4x4x1_16b_f32 v[48:51], v0, v0, 0
	v_mfma_f32_4x4x1_16b_f32 v[52:55], v0, v0, 0
	v_mfma_f32_4x4x1_16b_f32 v[56:59], v0, v0, 0
	v_mfma_f32_4x4x1_16b_f32 v[60:63], v0, v0, 0
	v_mfma_f32_4x4x1_16b_f32 v[64:67], v0, v0, 0
	v_mfma_f32_4x4x1_16b_f32 v[68:71], v0, v0, 0
	v_mfma_f32_4x4x1_16b_f32 v[72:75], v0, v0, 0
	v_mfma_f32_4x4x1_16b_f32 v[76:79], v0, v0, 0
	v_mfma_f32_4x4x1_16b_f32 v[80:83], v0, v0, 0
	v_mfma_f32_4x4x1_16b_f32 v[84:87], v0, v0, 0
	v_mfma_f32_4x4x1_16b_f32 v[88:91], v0, v0, 0
	v_mfma_f32_4x4x1_16b_f32 v[92:95], v0, v0, 0
	v_mfma_f32_4x4x1_16b_f32 v[96:99], v0, v0, 0
	v_mfma_f32_4x4x1_16b_f32 v[100:103], v0, v0, 0
	v_mfma_f32_4x4x1_16b_f32 v[104:107], v0, v0, 0
	v_mfma_f32_4x4x1_16b_f32 v[108:111], v0, v0, 0
	v_mfma_f32_4x4x1_16b_f32 v[112:115], v0, v0, 0
	v_mfma_f32_4x4x1_16b_f32 v[116:119], v0, v0, 0
	v_mfma_f32_4x4x1_16b_f32 v[120:123], v0, v0, 0
	v_mfma_f32_4x4x1_16b_f32 v[124:127], v0, v0, 0
	v_mfma_f32_4x4x1_16b_f32 v[0:3], v0, v0, 0
	s_nop 0
